# P0 fold: cos/-sin table value read with one unconditional ds_read_b32 (per-lane base and sign mask) instead of two exec-masked reads
# speedup vs baseline: 1.0048x; 1.0048x over previous
.LBB0_44:
	s_or_b64 exec, exec, s[44:45]
	v_mov_b32_e32 v120, 0x8100
	v_mov_b32_e32 v121, 0x8300
	v_mov_b32_e32 v122, 0
	v_bfrev_b32_e32 v123, 1
	v_cndmask_b32_e64 v120, v120, v121, s[8:9]
	v_cndmask_b32_e64 v121, v122, v123, s[8:9]
	v_mov_b32_e32 v10, 0
	v_mov_b32_e32 v55, 0
	s_mov_b32 s20, 0
	v_mov_b32_e32 v11, v10
	v_mov_b32_e32 v24, v10
	v_mov_b32_e32 v25, v10
	v_mov_b32_e32 v18, v10
	v_mov_b32_e32 v19, v10
	v_mov_b32_e32 v16, v10
	v_mov_b32_e32 v17, v10
	v_mov_b32_e32 v22, v10
	v_mov_b32_e32 v23, v10
	v_mov_b32_e32 v20, v10
	v_mov_b32_e32 v21, v10
	v_mov_b32_e32 v14, v10
	v_mov_b32_e32 v15, v10
	v_mov_b32_e32 v12, v10
	v_mov_b32_e32 v13, v10
	s_waitcnt lgkmcnt(0)
	s_barrier
	s_branch .LBB0_46
.LBB0_45:
	s_waitcnt lgkmcnt(5)
	v_xor_b32_e32 v26, v121, v26
	v_pk_fma_f32 v[22:23], v[26:27], v[40:41], v[22:23] op_sel_hi:[0,1,1]
	s_waitcnt lgkmcnt(4)
	v_pk_fma_f32 v[20:21], v[26:27], v[36:37], v[20:21] op_sel_hi:[0,1,1]
	s_waitcnt lgkmcnt(3)
	v_pk_fma_f32 v[14:15], v[26:27], v[34:35], v[14:15] op_sel_hi:[0,1,1]
	ds_read2_b32 v[34:35], v56 offset0:1 offset1:130
	ds_read2_b32 v[36:37], v63 offset0:3 offset1:132
	ds_read2_b32 v[40:41], v62 offset0:5 offset1:134
	v_pk_fma_f32 v[24:25], v[26:27], v[46:47], v[24:25] op_sel_hi:[0,1,1]
	v_pk_fma_f32 v[18:19], v[26:27], v[44:45], v[18:19] op_sel_hi:[0,1,1]
	v_pk_fma_f32 v[16:17], v[26:27], v[42:43], v[16:17] op_sel_hi:[0,1,1]
	s_waitcnt lgkmcnt(5)
	v_pk_fma_f32 v[12:13], v[26:27], v[30:31], v[12:13] op_sel_hi:[0,1,1]
	s_waitcnt lgkmcnt(3)
	v_pk_fma_f32 v[10:11], v[26:27], v[32:33], v[10:11] op_sel_hi:[0,1,1]
	s_waitcnt lgkmcnt(2)
	v_xor_b32_e32 v28, v121, v28
	v_pk_fma_f32 v[24:25], v[28:29], v[34:35], v[24:25] op_sel_hi:[0,1,1]
	s_waitcnt lgkmcnt(1)
	v_pk_fma_f32 v[18:19], v[28:29], v[36:37], v[18:19] op_sel_hi:[0,1,1]
	s_waitcnt lgkmcnt(0)
	v_pk_fma_f32 v[16:17], v[28:29], v[40:41], v[16:17] op_sel_hi:[0,1,1]
	ds_read2_b32 v[30:31], v61 offset0:7 offset1:136
	ds_read2_b32 v[32:33], v60 offset0:9 offset1:138
	ds_read2_b32 v[34:35], v59 offset0:11 offset1:140
	ds_read2_b32 v[36:37], v58 offset0:13 offset1:142
	ds_read_b32 v40, v56 offset:7228
	ds_read_b32 v41, v57 offset:4
	s_add_i32 s20, s20, 8
	s_waitcnt lgkmcnt(5)
	v_pk_fma_f32 v[22:23], v[28:29], v[30:31], v[22:23] op_sel_hi:[0,1,1]
	s_waitcnt lgkmcnt(4)
	v_pk_fma_f32 v[20:21], v[28:29], v[32:33], v[20:21] op_sel_hi:[0,1,1]
	s_waitcnt lgkmcnt(3)
	v_pk_fma_f32 v[14:15], v[28:29], v[34:35], v[14:15] op_sel_hi:[0,1,1]
	s_waitcnt lgkmcnt(2)
	v_pk_fma_f32 v[12:13], v[28:29], v[36:37], v[12:13] op_sel_hi:[0,1,1]
	s_waitcnt lgkmcnt(0)
	v_pk_fma_f32 v[10:11], v[28:29], v[40:41], v[10:11] op_sel_hi:[0,1,1]
	s_cmpk_eq_i32 s20, 0x200
	v_add_u32_e32 v55, v55, v53
	s_cbranch_scc1 .LBB0_29
.LBB0_46:
	v_and_b32_e32 v26, 0x7e, v55
	v_lshl_add_u32 v28, v26, 2, v120
	ds_read_b32 v26, v28
	v_add_u32_e32 v56, s20, v52
	v_add_u32_e32 v63, 0x400, v56
	v_add_u32_e32 v62, 0x800, v56
	v_add_u32_e32 v61, 0xc00, v56
	v_add_u32_e32 v60, 0x1000, v56
	v_add_u32_e32 v59, 0x1400, v56
	v_add_u32_e32 v58, 0x1800, v56
	ds_read2_b32 v[46:47], v56 offset1:129
	ds_read2_b32 v[44:45], v63 offset0:2 offset1:131
	ds_read2_b32 v[42:43], v62 offset0:4 offset1:133
	ds_read2_b32 v[40:41], v61 offset0:6 offset1:135
	ds_read2_b32 v[36:37], v60 offset0:8 offset1:137
	ds_read2_b32 v[34:35], v59 offset0:10 offset1:139
	ds_read2_b32 v[30:31], v58 offset0:12 offset1:141
	v_add_u32_e32 v57, s20, v51
	ds_read_b32 v32, v56 offset:7224
	ds_read_b32 v33, v57
	v_add_u32_e32 v28, v29, v55
	v_and_b32_e32 v28, 0x7f, v28
	v_lshl_add_u32 v64, v28, 2, v120
	ds_read_b32 v28, v64
	s_branch .LBB0_45
